# speedup vs baseline: 1.0041x; 1.0033x over previous
.LBB1_53:
	s_waitcnt vmcnt(0)
	v_cmp_ne_u32_e32 vcc, 0, v0
	s_lshr_b32 s0, vcc_lo, 16
	s_lshr_b32 s1, vcc_hi, 16
	s_or_b32 s0, s0, vcc_lo
	s_or_b32 s1, s1, vcc_hi
	s_or_b32 s0, s0, s1
	s_and_b32 s0, s0, 0xffff
	s_cmp_eq_u32 s0, 0
	s_cbranch_scc1 .LBB1_104
	v_lshrrev_b32_e64 v1, v100, s0
	v_and_b32_e32 v3, 15, v101
	v_and_b32_e32 v1, 1, v1
	v_add_u32_e32 v2, s16, v3
	v_cmp_ne_u32_e64 s[2:3], 0, v1
	v_cmp_eq_u32_e64 s[6:7], s45, v2
	v_cmp_eq_u32_e64 s[8:9], s46, v2
	s_and_b32 s38, s2, 0xffff
	s_flbit_i32_b32 s4, s38
	s_sub_u32 s5, 31, s4
	s_or_b64 s[6:7], s[6:7], s[8:9]
	v_cmp_le_u32_e64 s[12:13], s5, v3
	s_or_b64 s[6:7], s[6:7], s[20:21]
	v_add3_u32 v3, s33, v105, v102
	s_or_b64 s[6:7], s[6:7], s[12:13]
	s_and_b32 s1, s6, s38
	s_andn2_b32 s3, s38, s1
	v_add_u32_e32 v36, 0x8000, v3
	v_add_u32_e32 v37, 0x8800, v3
	v_add_u32_e32 v38, 0x9000, v3
	v_add_u32_e32 v39, 0x9800, v3
	ds_write2_b32 v36, v32, v28 offset1:16
	ds_write2_b32 v36, v24, v20 offset0:32 offset1:48
	ds_write2_b32 v36, v16, v12 offset0:64 offset1:80
	ds_write2_b32 v36, v8, v4 offset0:96 offset1:112
	ds_write2_b32 v37, v33, v29 offset1:16
	ds_write2_b32 v37, v25, v21 offset0:32 offset1:48
	ds_write2_b32 v37, v17, v13 offset0:64 offset1:80
	ds_write2_b32 v37, v9, v5 offset0:96 offset1:112
	ds_write2_b32 v38, v34, v30 offset1:16
	ds_write2_b32 v38, v26, v22 offset0:32 offset1:48
	ds_write2_b32 v38, v18, v14 offset0:64 offset1:80
	ds_write2_b32 v38, v10, v6 offset0:96 offset1:112
	ds_write2_b32 v39, v35, v31 offset1:16
	ds_write2_b32 v39, v27, v23 offset0:32 offset1:48
	ds_write2_b32 v39, v19, v15 offset0:64 offset1:80
	ds_write2_b32 v39, v11, v7 offset0:96 offset1:112
	s_mov_b32 s17, 0
	s_lshl_b64 s[14:15], s[16:17], 9
	s_add_u32 s14, s18, s14
	s_addc_u32 s15, s19, s15
	s_add_u32 s22, s14, 0x1000
	s_addc_u32 s23, s15, 0
	v_lshlrev_b32_e32 v40, 2, v101
	v_add_u32_e32 v41, s33, v40
	v_and_b32_e32 v2, 31, v101
	v_lshrrev_b32_e32 v1, 5, v101
	v_lshlrev_b32_e32 v2, 4, v2
	v_lshl_add_u32 v42, v1, 9, v2
	v_add_u32_e32 v43, s33, v42
	v_lshrrev_b32_e64 v76, v1, s3
	s_waitcnt lgkmcnt(0)
	ds_read_b128 v[44:47], v43 offset:32768
	ds_read_b128 v[48:51], v43 offset:33792
	ds_read_b128 v[52:55], v43 offset:34816
	ds_read_b128 v[56:59], v43 offset:35840
	ds_read_b128 v[60:63], v43 offset:36864
	ds_read_b128 v[64:67], v43 offset:37888
	ds_read_b128 v[68:71], v43 offset:38912
	ds_read_b128 v[72:75], v43 offset:39936
	v_mov_b32_e32 v78, v0
	v_mov_b32_e32 v79, v0
	s_nop 1
	v_permlane32_swap_b32_e32 v78, v79
	s_nop 1
	v_add_u32_e32 v78, v78, v79
	v_mov_b32_e32 v79, v78
	s_nop 1
	v_permlane16_swap_b32_e32 v78, v79
	s_nop 1
	v_add_u32_e32 v0, v78, v79
	v_cmp_ne_u32_e32 vcc, 0, v0
	s_and_b64 vcc, vcc, 0xffff
	s_and_saveexec_b64 s[24:25], vcc
	s_cbranch_execz .Lfl_nocnt
	s_mov_b32 s2, 0x24924925
	v_mul_hi_u32 v1, v0, s2
	v_sub_u32_e32 v0, v0, v1
	v_lshrrev_b32_e32 v0, 1, v0
	v_add_u32_e32 v0, v0, v1
	v_lshrrev_b32_e32 v0, 2, v0
	v_cvt_f32_u32_e32 v0, v0
	s_lshl_b64 s[26:27], s[16:17], 2
	s_add_u32 s26, s10, s26
	s_addc_u32 s27, s11, s27
	v_lshlrev_b32_e32 v1, 2, v100
	global_atomic_add_f32 v1, v0, s[26:27]
